# nt weight stores + K-loop placement (gate/up +40B, AB in-projection +40B, CD in-projection +20B, out-projection +28B)
# baseline (speedup 1.0000x reference)
; #define LAS __attribute__((address_space(3)))
; #define G8_STAGE(bufoff, gbase, voff) do { _Pragma("unroll") for (int _i = 0; _i < 2; ++_i) \
;         __builtin_amdgcn_global_load_lds((const unsigned*)((const char*)(gbase) + (voff)[_i]), (LAS unsigned*)(lds + (bufoff) + ldsw + _i * 8192), 16, 0, 0); } while (0)
; #define G8_WAIT_L(n) asm volatile("s_waitcnt lgkmcnt(" #n ")" ::: "memory")
; #define G8_BAR __builtin_amdgcn_s_barrier()
; #define G8_SCHED __builtin_amdgcn_sched_barrier(0)
; template <class Epi, class Sched>
; __device__ __forceinline__ void gemm_phase(LAS unsigned char* lds, const int K, const Sched& S, const Epi& E) {
;     ...
;         const bool has_next = S.next(ui + 1, nxt);
;         const char* nA = has_next ? nxt.A : cA; const char* nB = has_next ? nxt.B : cB;
; #pragma unroll 1
;         for (int t = 0; t < nt; t += 2) {
;             const bool last = (t == nt - 2);
;             const char* a1 = cA + (size_t)(t + 1) * kstep;
;             const char* a2 = last ? nA : cA + (size_t)(t + 2) * kstep; const char* b2 = last ? nB : cB + (size_t)(t + 2) * kstep;
;             const char* a3 = a2 + kstep; const char* b3 = b2 + kstep;
;             G8_LDB(B0, 0, 0); G8_SCHED; G8_LDA(At, 0, 0); G8_STAGE(G8_SA(1, 1), a1, oc[1]);
;             if (last && has_next) S.aoff(nxt, tid, oc);
;             G8_WAIT_L(8); G8_BAR; G8_WAIT_L(0); G8_MMA(0, 0, At, B0); G8_BAR; G8_SCHED;
;             G8_LDB(B1, 0, 1); G8_STAGE(G8_SB(0, 0), b2, voffB);
;             G8_BAR; G8_WAIT_L(0); G8_MMA(0, 1, At, B1); G8_BAR;
;             G8_LDA(At, 0, 1); G8_STAGE(G8_SA(0, 0), a2, oc[0]);
;             G8_BAR; G8_WAIT_L(0); G8_MMA(1, 0, At, B0); G8_BAR; G8_SCHED;
;     __device__ __forceinline__ void init(f32x4 (&acc)[2][2][4][2], const g8::Unit& u, int wc, int fq) const {
;         const int colp = u.pn * 256 + wc * 32 + fq * 8;
; #pragma unroll
;         for (int b = 0; b < 2; ++b)
; #pragma unroll
;             for (int n = 0; n < 2; ++n) { const u32x2 bw = *(const LAS u32x2*)(biasL + colp + b * 128 + 4 * n);
;                 const f32x4 bv = (f32x4){__uint_as_float(bw[0] << 16), __uint_as_float(bw[0] & 0xffff0000u), __uint_as_float(bw[1] << 16), __uint_as_float(bw[1] & 0xffff0000u)};
; #pragma unroll
;                 for (int a = 0; a < 2; ++a)
; #pragma unroll
;                     for (int m = 0; m < 4; ++m) acc[a][b][m][n] = bv; } }
.LBB0_486:
	v_mov_b64_e32 v[18:19], 0x440
	v_cmp_lt_i64_e64 s[34:35], s[34:35], v[18:19]
	s_add_u32 s3, s12, 0x100
	v_mov_b64_e32 v[20:21], v[8:9]
	v_mov_b64_e32 v[28:29], v[16:17]
	v_mov_b64_e32 v[36:37], v[8:9]
	v_mov_b64_e32 v[44:45], v[16:17]
	v_mov_b64_e32 v[52:53], v[8:9]
	v_mov_b64_e32 v[60:61], v[16:17]
	v_mov_b64_e32 v[24:25], v[4:5]
	v_mov_b64_e32 v[32:33], v[12:13]
	v_mov_b64_e32 v[40:41], v[4:5]
	v_mov_b64_e32 v[48:49], v[12:13]
	v_mov_b64_e32 v[56:57], v[4:5]
	v_mov_b64_e32 v[64:65], v[12:13]
	v_mov_b64_e32 v[68:69], v[8:9]
	v_mov_b64_e32 v[76:77], v[16:17]
	v_mov_b64_e32 v[84:85], v[8:9]
	v_mov_b64_e32 v[92:93], v[16:17]
	v_mov_b64_e32 v[100:101], v[8:9]
	v_mov_b64_e32 v[108:109], v[16:17]
	v_mov_b64_e32 v[116:117], v[8:9]
	v_mov_b64_e32 v[124:125], v[16:17]
	v_mov_b64_e32 v[72:73], v[4:5]
	v_mov_b64_e32 v[80:81], v[12:13]
	v_mov_b64_e32 v[88:89], v[4:5]
	v_mov_b64_e32 v[96:97], v[12:13]
	v_mov_b64_e32 v[104:105], v[4:5]
	v_mov_b64_e32 v[112:113], v[12:13]
	v_mov_b64_e32 v[120:121], v[4:5]
	v_mov_b64_e32 v[128:129], v[12:13]
	s_addc_u32 s14, s13, 0
	s_mov_b32 s47, -2
	v_mov_b64_e32 v[18:19], v[6:7]
	v_mov_b64_e32 v[26:27], v[14:15]
	v_mov_b64_e32 v[34:35], v[6:7]
	v_mov_b64_e32 v[42:43], v[14:15]
	v_mov_b64_e32 v[50:51], v[6:7]
	v_mov_b64_e32 v[58:59], v[14:15]
	v_mov_b64_e32 v[22:23], v[2:3]
	v_mov_b64_e32 v[30:31], v[10:11]
	v_mov_b64_e32 v[38:39], v[2:3]
	v_mov_b64_e32 v[46:47], v[10:11]
	v_mov_b64_e32 v[54:55], v[2:3]
	v_mov_b64_e32 v[62:63], v[10:11]
	v_mov_b64_e32 v[66:67], v[6:7]
	v_mov_b64_e32 v[74:75], v[14:15]
	v_mov_b64_e32 v[82:83], v[6:7]
	v_mov_b64_e32 v[90:91], v[14:15]
	v_mov_b64_e32 v[98:99], v[6:7]
	v_mov_b64_e32 v[106:107], v[14:15]
	v_mov_b64_e32 v[114:115], v[6:7]
	v_mov_b64_e32 v[122:123], v[14:15]
	v_mov_b64_e32 v[70:71], v[2:3]
	v_mov_b64_e32 v[78:79], v[10:11]
	v_mov_b64_e32 v[86:87], v[2:3]
	v_mov_b64_e32 v[94:95], v[10:11]
	v_mov_b64_e32 v[102:103], v[2:3]
	v_mov_b64_e32 v[110:111], v[10:11]
	v_mov_b64_e32 v[118:119], v[2:3]
	v_mov_b64_e32 v[126:127], v[10:11]
	s_nop 0
	s_nop 0
	s_nop 0
	s_nop 0
	s_nop 0
	s_nop 0
	s_nop 0
	s_nop 0
	s_nop 0
	s_nop 0
.LBB0_487:
	s_add_u32 s12, s0, 0x100
	s_addc_u32 s13, s1, 0
	s_add_i32 s49, 0, 0x10000
	v_add_u32_e32 v158, s49, v165
	ds_read_b128 v[130:133], v158
	ds_read_b128 v[134:137], v158 offset:1024
	ds_read_b128 v[154:157], v158 offset:2048
	ds_read_b128 v[158:161], v158 offset:3072
	s_cmp_eq_u32 s47, 12
	s_cselect_b32 s43, s23, s13
	s_cselect_b32 s42, s22, s12
	s_cselect_b32 s39, s37, s14
	s_cselect_b32 s38, s36, s3
	v_lshl_add_u64 v[162:163], s[0:1], 0, v[152:153]
	s_add_i32 m0, s76, 0xc000
	ds_read_b128 v[168:171], v167
	ds_read_b128 v[172:175], v167 offset:1024
	ds_read_b128 v[176:179], v167 offset:2048
	ds_read_b128 v[180:183], v167 offset:3072
	ds_read_b128 v[184:187], v167 offset:4096
	ds_read_b128 v[188:191], v167 offset:5120
	ds_read_b128 v[192:195], v167 offset:6144
	ds_read_b128 v[196:199], v167 offset:7168
	global_load_lds_dwordx4 v[162:163], off
	v_lshl_add_u64 v[162:163], s[0:1], 0, v[150:151]
	s_add_i32 m0, s76, 0xe000
	s_nop 0
	global_load_lds_dwordx4 v[162:163], off
	s_waitcnt lgkmcnt(8)
	s_barrier
	s_waitcnt lgkmcnt(0)
	s_setprio 1
	s_waitcnt lgkmcnt(0)
	v_mfma_f32_16x16x32_bf16 v[126:129], v[130:133], v[168:171], v[126:129]
	v_mfma_f32_16x16x32_bf16 v[118:121], v[154:157], v[168:171], v[118:121]
	v_mfma_f32_16x16x32_bf16 v[110:113], v[130:133], v[176:179], v[110:113]
	v_mfma_f32_16x16x32_bf16 v[102:105], v[154:157], v[176:179], v[102:105]
	v_mfma_f32_16x16x32_bf16 v[94:97], v[130:133], v[184:187], v[94:97]
	v_mfma_f32_16x16x32_bf16 v[86:89], v[154:157], v[184:187], v[86:89]
	v_mfma_f32_16x16x32_bf16 v[78:81], v[130:133], v[192:195], v[78:81]
	v_mfma_f32_16x16x32_bf16 v[70:73], v[154:157], v[192:195], v[70:73]
	v_mfma_f32_16x16x32_bf16 v[126:129], v[134:137], v[172:175], v[126:129]
	v_mfma_f32_16x16x32_bf16 v[118:121], v[158:161], v[172:175], v[118:121]
	v_mfma_f32_16x16x32_bf16 v[110:113], v[134:137], v[180:183], v[110:113]
	v_mfma_f32_16x16x32_bf16 v[102:105], v[158:161], v[180:183], v[102:105]
	v_mfma_f32_16x16x32_bf16 v[94:97], v[134:137], v[188:191], v[94:97]
	v_mfma_f32_16x16x32_bf16 v[86:89], v[158:161], v[188:191], v[86:89]
	v_mfma_f32_16x16x32_bf16 v[78:81], v[134:137], v[196:199], v[78:81]
	v_mfma_f32_16x16x32_bf16 v[70:73], v[158:161], v[196:199], v[70:73]
	s_setprio 0
	s_barrier
	s_add_i32 s54, 0, 0x14000
	v_add_u32_e32 v162, s54, v165
	s_add_i32 s0, s49, s65
	ds_read_b128 v[216:219], v162
	ds_read_b128 v[220:223], v162 offset:1024
	ds_read_b128 v[224:227], v162 offset:2048
	ds_read_b128 v[228:231], v162 offset:3072
	v_lshl_add_u64 v[162:163], s[38:39], 0, v[0:1]
	s_mov_b32 m0, s0
	v_lshl_add_u64 v[200:201], s[38:39], 0, v[140:141]
	global_load_lds_dwordx4 v[162:163], off
	s_add_i32 m0, s0, 0x2000
	s_nop 0
	global_load_lds_dwordx4 v[200:201], off
	s_barrier
	s_waitcnt lgkmcnt(0)
	s_setprio 1
	s_waitcnt lgkmcnt(0)
	v_mfma_f32_16x16x32_bf16 v[122:125], v[216:219], v[168:171], v[122:125]
	v_mfma_f32_16x16x32_bf16 v[114:117], v[224:227], v[168:171], v[114:117]
	v_mfma_f32_16x16x32_bf16 v[106:109], v[216:219], v[176:179], v[106:109]
	v_mfma_f32_16x16x32_bf16 v[98:101], v[224:227], v[176:179], v[98:101]
	v_mfma_f32_16x16x32_bf16 v[90:93], v[216:219], v[184:187], v[90:93]
	v_mfma_f32_16x16x32_bf16 v[82:85], v[224:227], v[184:187], v[82:85]
	v_mfma_f32_16x16x32_bf16 v[74:77], v[216:219], v[192:195], v[74:77]
	v_mfma_f32_16x16x32_bf16 v[66:69], v[224:227], v[192:195], v[66:69]
	v_mfma_f32_16x16x32_bf16 v[122:125], v[220:223], v[172:175], v[122:125]
	v_mfma_f32_16x16x32_bf16 v[114:117], v[228:231], v[172:175], v[114:117]
	v_mfma_f32_16x16x32_bf16 v[106:109], v[220:223], v[180:183], v[106:109]
	v_mfma_f32_16x16x32_bf16 v[98:101], v[228:231], v[180:183], v[98:101]
	v_mfma_f32_16x16x32_bf16 v[90:93], v[220:223], v[188:191], v[90:93]
	v_mfma_f32_16x16x32_bf16 v[82:85], v[228:231], v[188:191], v[82:85]
	v_mfma_f32_16x16x32_bf16 v[74:77], v[220:223], v[196:199], v[74:77]
	v_mfma_f32_16x16x32_bf16 v[66:69], v[228:231], v[196:199], v[66:69]
	s_setprio 0
	s_mov_b32 m0, s76
	v_lshl_add_u64 v[232:233], s[42:43], 0, v[142:143]
	s_barrier
; #define G8_STAGE(bufoff, gbase, voff) do { _Pragma("unroll") for (int _i = 0; _i < 2; ++_i) \
;         __builtin_amdgcn_global_load_lds((const unsigned*)((const char*)(gbase) + (voff)[_i]), (LAS unsigned*)(lds + (bufoff) + ldsw + _i * 8192), 16, 0, 0); } while (0)
; #define G8_LDA(dst, b, h) do { _Pragma("unroll") for (int m = 0; m < 4; ++m) _Pragma("unroll") for (int k = 0; k < 2; ++k) dst[m][k] = *(const LAS bf16x8*)(lds + G8_SA(b, h) + aoff + m * 2048 + k * 1024); } while (0)
; #define G8_LDB(dst, b, h) do { _Pragma("unroll") for (int n = 0; n < 2; ++n) _Pragma("unroll") for (int k = 0; k < 2; ++k) dst[n][k] = *(const LAS bf16x8*)(lds + G8_SB(b, h) + boff + n * 2048 + k * 1024); } while (0)
; #define G8_MMA(ai, bj, At, Bt) do { __builtin_amdgcn_s_setprio(1); _Pragma("unroll") for (int m = 0; m < 4; ++m) _Pragma("unroll") for (int n = 0; n < 2; ++n) _Pragma("unroll") for (int k = 0; k < 2; ++k) \
;         acc[ai][bj][m][n] = __builtin_amdgcn_mfma_f32_16x16x32_bf16(Bt[n][k], At[m][k], acc[ai][bj][m][n], 0, 0, 0); __builtin_amdgcn_s_setprio(0); } while (0)
; #define G8_WAIT_V(n) asm volatile("s_waitcnt vmcnt(" #n ")" ::: "memory")
; #define G8_WAIT_L(n) asm volatile("s_waitcnt lgkmcnt(" #n ")" ::: "memory")
; #define G8_BAR __builtin_amdgcn_s_barrier()
; #define G8_SCHED __builtin_amdgcn_sched_barrier(0)
; template <class Epi, class Sched>
; __device__ __forceinline__ void gemm_phase(LAS unsigned char* lds, const int K, const Sched& S, const Epi& E) {
;     ...
;             G8_STAGE(G8_SB(0, 1), b2 + hstep, voffB);
;             G8_WAIT_V(6); G8_BAR; G8_MMA(1, 1, At, B1); G8_BAR;
;             G8_LDB(B0, 1, 0); G8_SCHED; G8_LDA(At, 1, 0); G8_STAGE(G8_SA(0, 1), a2, oc[1]);
;             G8_WAIT_L(8); G8_BAR; G8_WAIT_L(0); G8_MMA(0, 0, At, B0); G8_BAR; G8_SCHED;
;             G8_LDB(B1, 1, 1); G8_STAGE(G8_SB(1, 0), b3, voffB);
;             G8_BAR; G8_WAIT_L(0); G8_MMA(0, 1, At, B1); G8_BAR;
;             G8_LDA(At, 1, 1); G8_STAGE(G8_SA(1, 0), a3, oc[0]);
	ds_read_b128 v[168:171], v167 offset:16384
	ds_read_b128 v[172:175], v167 offset:17408
	ds_read_b128 v[176:179], v167 offset:18432
	ds_read_b128 v[180:183], v167 offset:19456
	ds_read_b128 v[184:187], v167 offset:20480
	ds_read_b128 v[188:191], v167 offset:21504
	ds_read_b128 v[192:195], v167 offset:22528
	ds_read_b128 v[196:199], v167 offset:23552
	global_load_lds_dwordx4 v[232:233], off
	v_lshl_add_u64 v[234:235], s[42:43], 0, v[146:147]
	s_mov_b32 m0, s77
	s_nop 0
	global_load_lds_dwordx4 v[234:235], off
	s_barrier
	s_waitcnt lgkmcnt(0)
	s_setprio 1
	s_waitcnt lgkmcnt(0)
	v_mfma_f32_16x16x32_bf16 v[62:65], v[130:133], v[168:171], v[62:65]
	v_mfma_f32_16x16x32_bf16 v[54:57], v[154:157], v[168:171], v[54:57]
	v_mfma_f32_16x16x32_bf16 v[46:49], v[130:133], v[176:179], v[46:49]
	v_mfma_f32_16x16x32_bf16 v[38:41], v[154:157], v[176:179], v[38:41]
	v_mfma_f32_16x16x32_bf16 v[30:33], v[130:133], v[184:187], v[30:33]
	v_mfma_f32_16x16x32_bf16 v[22:25], v[154:157], v[184:187], v[22:25]
	v_mfma_f32_16x16x32_bf16 v[10:13], v[130:133], v[192:195], v[10:13]
	v_mfma_f32_16x16x32_bf16 v[2:5], v[154:157], v[192:195], v[2:5]
	v_mfma_f32_16x16x32_bf16 v[62:65], v[134:137], v[172:175], v[62:65]
	v_mfma_f32_16x16x32_bf16 v[54:57], v[158:161], v[172:175], v[54:57]
	v_mfma_f32_16x16x32_bf16 v[46:49], v[134:137], v[180:183], v[46:49]
	v_mfma_f32_16x16x32_bf16 v[38:41], v[158:161], v[180:183], v[38:41]
	v_mfma_f32_16x16x32_bf16 v[30:33], v[134:137], v[188:191], v[30:33]
	v_mfma_f32_16x16x32_bf16 v[22:25], v[158:161], v[188:191], v[22:25]
	v_mfma_f32_16x16x32_bf16 v[10:13], v[134:137], v[196:199], v[10:13]
	v_mfma_f32_16x16x32_bf16 v[2:5], v[158:161], v[196:199], v[2:5]
	s_setprio 0
	s_barrier
	s_add_u32 s0, s38, 0x40000
	s_addc_u32 s1, s39, 0
	s_add_i32 s49, s54, s65
	v_lshl_add_u64 v[130:131], s[0:1], 0, v[0:1]
	s_mov_b32 m0, s49
	s_nop 0
	global_load_lds_dwordx4 v[130:131], off
	v_lshl_add_u64 v[130:131], s[0:1], 0, v[140:141]
	s_add_i32 m0, s49, 0x2000
	s_nop 0
	global_load_lds_dwordx4 v[130:131], off
	s_waitcnt vmcnt(6)
	s_barrier
	s_setprio 1
	v_mfma_f32_16x16x32_bf16 v[58:61], v[216:219], v[168:171], v[58:61]
	v_mfma_f32_16x16x32_bf16 v[50:53], v[224:227], v[168:171], v[50:53]
	v_mfma_f32_16x16x32_bf16 v[42:45], v[216:219], v[176:179], v[42:45]
	v_mfma_f32_16x16x32_bf16 v[34:37], v[224:227], v[176:179], v[34:37]
	v_mfma_f32_16x16x32_bf16 v[26:29], v[216:219], v[184:187], v[26:29]
	v_mfma_f32_16x16x32_bf16 v[18:21], v[224:227], v[184:187], v[18:21]
	v_mfma_f32_16x16x32_bf16 v[14:17], v[216:219], v[192:195], v[14:17]
	v_mfma_f32_16x16x32_bf16 v[6:9], v[224:227], v[192:195], v[6:9]
	v_mfma_f32_16x16x32_bf16 v[58:61], v[220:223], v[172:175], v[58:61]
	v_mfma_f32_16x16x32_bf16 v[50:53], v[228:231], v[172:175], v[50:53]
	v_mfma_f32_16x16x32_bf16 v[42:45], v[220:223], v[180:183], v[42:45]
	v_mfma_f32_16x16x32_bf16 v[34:37], v[228:231], v[180:183], v[34:37]
	v_mfma_f32_16x16x32_bf16 v[26:29], v[220:223], v[188:191], v[26:29]
	v_mfma_f32_16x16x32_bf16 v[18:21], v[228:231], v[188:191], v[18:21]
	v_mfma_f32_16x16x32_bf16 v[14:17], v[220:223], v[196:199], v[14:17]
	v_mfma_f32_16x16x32_bf16 v[6:9], v[228:231], v[196:199], v[6:9]
	s_setprio 0
	s_add_i32 s0, 0, 0x18000
	v_add_u32_e32 v158, s0, v165
	s_barrier
	ds_read_b128 v[130:133], v158
	ds_read_b128 v[134:137], v158 offset:1024
	ds_read_b128 v[154:157], v158 offset:2048
	ds_read_b128 v[158:161], v158 offset:3072
	s_mov_b32 m0, s78
	v_lshl_add_u64 v[216:217], s[42:43], 0, v[144:145]
	ds_read_b128 v[168:171], v167 offset:32768
	ds_read_b128 v[172:175], v167 offset:33792
	ds_read_b128 v[176:179], v167 offset:34816
	ds_read_b128 v[180:183], v167 offset:35840
	ds_read_b128 v[184:187], v167 offset:36864
	ds_read_b128 v[188:191], v167 offset:37888
	ds_read_b128 v[192:195], v167 offset:38912
	ds_read_b128 v[196:199], v167 offset:39936
	global_load_lds_dwordx4 v[216:217], off
	v_lshl_add_u64 v[216:217], s[42:43], 0, v[148:149]
	s_mov_b32 m0, s79
	s_nop 0
	global_load_lds_dwordx4 v[216:217], off
	s_waitcnt lgkmcnt(8)
	s_barrier
	s_waitcnt lgkmcnt(0)
	s_setprio 1
	s_waitcnt lgkmcnt(0)
	v_mfma_f32_16x16x32_bf16 v[126:129], v[130:133], v[168:171], v[126:129]
	v_mfma_f32_16x16x32_bf16 v[118:121], v[154:157], v[168:171], v[118:121]
	v_mfma_f32_16x16x32_bf16 v[110:113], v[130:133], v[176:179], v[110:113]
	v_mfma_f32_16x16x32_bf16 v[102:105], v[154:157], v[176:179], v[102:105]
	v_mfma_f32_16x16x32_bf16 v[94:97], v[130:133], v[184:187], v[94:97]
	v_mfma_f32_16x16x32_bf16 v[86:89], v[154:157], v[184:187], v[86:89]
	v_mfma_f32_16x16x32_bf16 v[78:81], v[130:133], v[192:195], v[78:81]
	v_mfma_f32_16x16x32_bf16 v[70:73], v[154:157], v[192:195], v[70:73]
	v_mfma_f32_16x16x32_bf16 v[126:129], v[134:137], v[172:175], v[126:129]
	v_mfma_f32_16x16x32_bf16 v[118:121], v[158:161], v[172:175], v[118:121]
	v_mfma_f32_16x16x32_bf16 v[110:113], v[134:137], v[180:183], v[110:113]
	v_mfma_f32_16x16x32_bf16 v[102:105], v[158:161], v[180:183], v[102:105]
	v_mfma_f32_16x16x32_bf16 v[94:97], v[134:137], v[188:191], v[94:97]
	v_mfma_f32_16x16x32_bf16 v[86:89], v[158:161], v[188:191], v[86:89]
	v_mfma_f32_16x16x32_bf16 v[78:81], v[134:137], v[196:199], v[78:81]
	v_mfma_f32_16x16x32_bf16 v[70:73], v[158:161], v[196:199], v[70:73]
	s_setprio 0
	s_barrier
	s_add_i32 s42, 0, 0x1c000
	s_add_i32 s0, s0, s65
	v_add_u32_e32 v213, s42, v165
	v_lshl_add_u64 v[162:163], v[162:163], 0, s[18:19]
	s_mov_b32 m0, s0
	ds_read_b128 v[216:219], v213
	ds_read_b128 v[220:223], v213 offset:1024
	ds_read_b128 v[224:227], v213 offset:2048
	ds_read_b128 v[228:231], v213 offset:3072
	global_load_lds_dwordx4 v[162:163], off
	v_lshl_add_u64 v[162:163], v[200:201], 0, s[18:19]
	s_add_i32 m0, s0, 0x2000
	s_nop 0
	global_load_lds_dwordx4 v[162:163], off
	s_barrier
; #define G8_STAGE(bufoff, gbase, voff) do { _Pragma("unroll") for (int _i = 0; _i < 2; ++_i) \
;         __builtin_amdgcn_global_load_lds((const unsigned*)((const char*)(gbase) + (voff)[_i]), (LAS unsigned*)(lds + (bufoff) + ldsw + _i * 8192), 16, 0, 0); } while (0)
; #define G8_LDA(dst, b, h) do { _Pragma("unroll") for (int m = 0; m < 4; ++m) _Pragma("unroll") for (int k = 0; k < 2; ++k) dst[m][k] = *(const LAS bf16x8*)(lds + G8_SA(b, h) + aoff + m * 2048 + k * 1024); } while (0)
; #define G8_MMA(ai, bj, At, Bt) do { __builtin_amdgcn_s_setprio(1); _Pragma("unroll") for (int m = 0; m < 4; ++m) _Pragma("unroll") for (int n = 0; n < 2; ++n) _Pragma("unroll") for (int k = 0; k < 2; ++k) \
;         acc[ai][bj][m][n] = __builtin_amdgcn_mfma_f32_16x16x32_bf16(Bt[n][k], At[m][k], acc[ai][bj][m][n], 0, 0, 0); __builtin_amdgcn_s_setprio(0); } while (0)
; #define G8_WAIT_V(n) asm volatile("s_waitcnt vmcnt(" #n ")" ::: "memory")
; #define G8_WAIT_L(n) asm volatile("s_waitcnt lgkmcnt(" #n ")" ::: "memory")
; #define G8_BAR __builtin_amdgcn_s_barrier()
; #define G8_SCHED __builtin_amdgcn_sched_barrier(0)
; template <class Epi, class Sched>
; __device__ __forceinline__ void gemm_phase(LAS unsigned char* lds, const int K, const Sched& S, const Epi& E) {
;     ...
;             G8_BAR; G8_WAIT_L(0); G8_MMA(0, 1, At, B1); G8_BAR;
;             G8_LDA(At, 1, 1); G8_STAGE(G8_SA(1, 0), a3, oc[0]);
;             G8_BAR; G8_WAIT_L(0); G8_MMA(1, 0, At, B0); G8_BAR; G8_SCHED;
;             G8_STAGE(G8_SB(1, 1), b3 + hstep, voffB);
;             G8_WAIT_V(6); G8_BAR; G8_MMA(1, 1, At, B1); G8_BAR;
;         }
	s_waitcnt lgkmcnt(0)
	s_setprio 1
	s_waitcnt lgkmcnt(0)
	v_mfma_f32_16x16x32_bf16 v[122:125], v[216:219], v[168:171], v[122:125]
	v_mfma_f32_16x16x32_bf16 v[114:117], v[224:227], v[168:171], v[114:117]
	v_mfma_f32_16x16x32_bf16 v[106:109], v[216:219], v[176:179], v[106:109]
	v_mfma_f32_16x16x32_bf16 v[98:101], v[224:227], v[176:179], v[98:101]
	v_mfma_f32_16x16x32_bf16 v[90:93], v[216:219], v[184:187], v[90:93]
	v_mfma_f32_16x16x32_bf16 v[82:85], v[224:227], v[184:187], v[82:85]
	v_mfma_f32_16x16x32_bf16 v[74:77], v[216:219], v[192:195], v[74:77]
	v_mfma_f32_16x16x32_bf16 v[66:69], v[224:227], v[192:195], v[66:69]
	v_mfma_f32_16x16x32_bf16 v[122:125], v[220:223], v[172:175], v[122:125]
	v_mfma_f32_16x16x32_bf16 v[114:117], v[228:231], v[172:175], v[114:117]
	v_mfma_f32_16x16x32_bf16 v[106:109], v[220:223], v[180:183], v[106:109]
	v_mfma_f32_16x16x32_bf16 v[98:101], v[228:231], v[180:183], v[98:101]
	v_mfma_f32_16x16x32_bf16 v[90:93], v[220:223], v[188:191], v[90:93]
	v_mfma_f32_16x16x32_bf16 v[82:85], v[228:231], v[188:191], v[82:85]
	v_mfma_f32_16x16x32_bf16 v[74:77], v[220:223], v[196:199], v[74:77]
	v_mfma_f32_16x16x32_bf16 v[66:69], v[228:231], v[196:199], v[66:69]
	s_setprio 0
	s_mov_b32 m0, s81
	v_lshl_add_u64 v[162:163], v[232:233], 0, s[18:19]
	s_barrier
	ds_read_b128 v[168:171], v167 offset:49152
	ds_read_b128 v[172:175], v167 offset:50176
	ds_read_b128 v[176:179], v167 offset:51200
	ds_read_b128 v[180:183], v167 offset:52224
	ds_read_b128 v[184:187], v167 offset:53248
	ds_read_b128 v[188:191], v167 offset:54272
	ds_read_b128 v[192:195], v167 offset:55296
	ds_read_b128 v[196:199], v167 offset:56320
	global_load_lds_dwordx4 v[162:163], off
	v_lshl_add_u64 v[162:163], v[234:235], 0, s[18:19]
	s_mov_b32 m0, s82
	s_nop 0
	global_load_lds_dwordx4 v[162:163], off
	s_barrier
	s_waitcnt lgkmcnt(0)
	s_setprio 1
	s_waitcnt lgkmcnt(0)
	v_mfma_f32_16x16x32_bf16 v[62:65], v[130:133], v[168:171], v[62:65]
	v_mfma_f32_16x16x32_bf16 v[54:57], v[154:157], v[168:171], v[54:57]
	v_mfma_f32_16x16x32_bf16 v[46:49], v[130:133], v[176:179], v[46:49]
	v_mfma_f32_16x16x32_bf16 v[38:41], v[154:157], v[176:179], v[38:41]
	v_mfma_f32_16x16x32_bf16 v[30:33], v[130:133], v[184:187], v[30:33]
	v_mfma_f32_16x16x32_bf16 v[22:25], v[154:157], v[184:187], v[22:25]
	v_mfma_f32_16x16x32_bf16 v[10:13], v[130:133], v[192:195], v[10:13]
	v_mfma_f32_16x16x32_bf16 v[2:5], v[154:157], v[192:195], v[2:5]
	v_mfma_f32_16x16x32_bf16 v[62:65], v[134:137], v[172:175], v[62:65]
	v_mfma_f32_16x16x32_bf16 v[54:57], v[158:161], v[172:175], v[54:57]
	v_mfma_f32_16x16x32_bf16 v[46:49], v[134:137], v[180:183], v[46:49]
	v_mfma_f32_16x16x32_bf16 v[38:41], v[158:161], v[180:183], v[38:41]
	v_mfma_f32_16x16x32_bf16 v[30:33], v[134:137], v[188:191], v[30:33]
	v_mfma_f32_16x16x32_bf16 v[22:25], v[158:161], v[188:191], v[22:25]
	v_mfma_f32_16x16x32_bf16 v[10:13], v[134:137], v[196:199], v[10:13]
	v_mfma_f32_16x16x32_bf16 v[2:5], v[158:161], v[196:199], v[2:5]
	s_setprio 0
	s_barrier
	s_add_u32 s0, s38, 0x40080
	s_addc_u32 s1, s39, 0
	s_add_i32 s38, s42, s65
	v_lshl_add_u64 v[130:131], s[0:1], 0, v[0:1]
	s_mov_b32 m0, s38
	s_nop 0
	global_load_lds_dwordx4 v[130:131], off
	v_lshl_add_u64 v[130:131], s[0:1], 0, v[140:141]
	s_add_i32 m0, s38, 0x2000
	s_nop 0
	global_load_lds_dwordx4 v[130:131], off
	s_waitcnt vmcnt(6)
	s_barrier
	s_setprio 1
	v_mfma_f32_16x16x32_bf16 v[58:61], v[216:219], v[168:171], v[58:61]
	v_mfma_f32_16x16x32_bf16 v[50:53], v[224:227], v[168:171], v[50:53]
	v_mfma_f32_16x16x32_bf16 v[42:45], v[216:219], v[176:179], v[42:45]
	v_mfma_f32_16x16x32_bf16 v[34:37], v[224:227], v[176:179], v[34:37]
	v_mfma_f32_16x16x32_bf16 v[26:29], v[216:219], v[184:187], v[26:29]
	v_mfma_f32_16x16x32_bf16 v[18:21], v[224:227], v[184:187], v[18:21]
	v_mfma_f32_16x16x32_bf16 v[14:17], v[216:219], v[192:195], v[14:17]
	v_mfma_f32_16x16x32_bf16 v[6:9], v[224:227], v[192:195], v[6:9]
	v_mfma_f32_16x16x32_bf16 v[58:61], v[220:223], v[172:175], v[58:61]
	v_mfma_f32_16x16x32_bf16 v[50:53], v[228:231], v[172:175], v[50:53]
	v_mfma_f32_16x16x32_bf16 v[42:45], v[220:223], v[180:183], v[42:45]
	v_mfma_f32_16x16x32_bf16 v[34:37], v[228:231], v[180:183], v[34:37]
	v_mfma_f32_16x16x32_bf16 v[26:29], v[220:223], v[188:191], v[26:29]
	v_mfma_f32_16x16x32_bf16 v[18:21], v[228:231], v[188:191], v[18:21]
	v_mfma_f32_16x16x32_bf16 v[14:17], v[220:223], v[196:199], v[14:17]
	v_mfma_f32_16x16x32_bf16 v[6:9], v[228:231], v[196:199], v[6:9]
	s_setprio 0
	s_add_i32 s47, s47, 2
	s_add_u32 s3, s3, 0x100
	s_addc_u32 s14, s14, 0
	s_cmp_gt_u32 s47, 13
	s_mov_b64 s[0:1], s[12:13]
	s_barrier
	s_cbranch_scc0 .LBB0_487
;     __device__ __forceinline__ void operator()(const f32x4 (&acc)[2][2][4][2], const g8::Unit& u, int wr, int wc, int fr_, int fq_) const {
;         int fr = fr_, fq = fq_; asm volatile("" : "+v"(fr), "+v"(fq));
;         const int pn = u.pn; const int colp = pn * 256 + wc * 32 + fq * 8;
;         bf16_t* qb = (bf16_t*)(ws + AB_QB); bf16_t* kb = (bf16_t*)(ws + AB_KB); bf16_t* vT = (bf16_t*)(ws + AB_VT); bf16_t* rqb = (bf16_t*)(ws + AB_RQB); bf16_t* rkb = (bf16_t*)(ws + AB_RKB);
;         bf16_t* rkdT = (bf16_t*)(ws + AB_RKDT); bf16_t* rvT = (bf16_t*)(ws + AB_RVT); bf16_t* rgb = (bf16_t*)(ws + AB_RGB);
;         const float frqA0 = exp2f(-(float)(fq * 8) * (13.287712379549449f / 32.f)) * 0.15915494309189535f;
;         const float frqR0 = exp2f(-(float)((wc & 1) * 32 + fq * 8) * (13.287712379549449f / 63.f)) * 0.15915494309189535f;
;         constexpr float RA[8] = {1.f, 0.7498942093324559f, 0.5623413251903491f, 0.4216965034285822f, 0.31622776601683794f, 0.23713737056616552f, 0.1778279410038923f, 0.1333521432163324f};
;         constexpr float RR[8] = {1.f, 0.8639884494839686f, 0.746476040841712f, 0.6449466771037624f, 0.5572264795507174f, 0.4814372420784346f, 0.4159562163071847f, 0.35938136638046275f};
; #pragma unroll
;         for (int ai = 0; ai < 2; ++ai)
; #pragma unroll
;             for (int m = 0; m < 4; ++m) {
;                 const int t = u.pm * 256 + ai * 128 + wr * 64 + m * 16 + fr, sq = t & (SEQ - 1), b = t >> 13;
;                 f32x4 x[2][2];
; #pragma unroll
;                 for (int bj = 0; bj < 2; ++bj)
; #pragma unroll
;                     for (int n = 0; n < 2; ++n) x[bj][n] = acc[ai][bj][m][n];
;                 if (pn < 4 || (pn == 4 && wc < 2)) {
;                     const int j0 = fq * 8; const float sc = pn < 4 ? 0.125f : 1.f;
;                     u32x4 w1, w2;
; #pragma unroll
;                     for (int n = 0; n < 2; ++n) { f32x4 o1, o2;
; #pragma unroll
;                         for (int e = 0; e < 4; ++e) { const float rev = __builtin_amdgcn_fractf((float)sq * (frqA0 * RA[4 * n + e])); const float cc = __builtin_amdgcn_cosf(rev) * sc, ss = __builtin_amdgcn_sinf(rev) * sc;
;                             o1[e] = x[0][n][e] * cc - x[1][n][e] * ss; o2[e] = x[1][n][e] * cc + x[0][n][e] * ss; }
	s_nop 0
	s_nop 0
	s_nop 0
	s_nop 0
	s_nop 0
	s_nop 0
	s_lshl_b32 s2, s2, 8
	s_add_i32 s2, s2, s80
	s_cmp_lt_i32 s94, 4
	s_cselect_b64 s[36:37], -1, 0
	s_cmp_lg_u32 s94, 4
	v_mov_b32_e32 v131, v164
	v_mov_b32_e32 v130, v139
	s_cselect_b64 s[12:13], -1, 0
	s_cmp_eq_u32 s94, 4
	s_nop 0
	v_add_u32_e32 v160, s2, v131
	s_cselect_b64 s[2:3], -1, 0
	s_and_b64 s[2:3], s[2:3], s[10:11]
	s_cmp_gt_u32 s94, 8
	s_cselect_b64 s[56:57], -1, 0
	s_cmp_gt_u32 s94, 12
	s_cselect_b64 s[54:55], -1, 0
	s_lshl_b32 s42, s94, 8
	s_add_i32 s14, s42, 0xfffff300
	v_lshlrev_b32_e32 v130, 3, v130
	s_lshl_b64 s[22:23], s[14:15], 1
	v_add_u32_e32 v132, s85, v130
	s_add_u32 s22, s87, s22
	v_cvt_f32_i32_e32 v133, v132
	s_addc_u32 s23, s88, s23
	s_add_i32 s14, s86, s42
	s_cmp_gt_u32 s94, 6
	v_add_u32_e32 v171, s14, v130
	s_cselect_b64 s[38:39], -1, 0
	s_lshl_b32 s14, s94, 1
	s_and_b32 s14, s14, 2
	v_mul_f32_e32 v134, 0xbe57fa62, v133
	s_or_b32 s14, s14, s89
	v_cmp_gt_f32_e32 vcc, s66, v134
	v_ashrrev_i32_e32 v131, 31, v130
	s_lshl_b32 s14, s14, 7
	v_cvt_f32_i32_e32 v172, v130
	v_cndmask_b32_e32 v134, 0, v207, vcc
	v_lshlrev_b64 v[162:163], 1, v[130:131]
	s_xor_b32 s14, s14, 0x100
	v_fmac_f32_e32 v134, 0xbe57fa62, v133
	v_lshl_add_u64 v[158:159], s[22:23], 0, v[162:163]
	s_and_b64 s[22:23], s[38:39], exec
	v_exp_f32_e32 v133, v134
	s_mov_b32 s22, 0x3d420000
	s_cselect_b32 s22, s22, 0x3c420000
	v_mul_f32_e32 v134, 0xbed49a78, v172
	s_add_u32 s22, s40, s22
	v_cmp_gt_f32_e64 s[0:1], s66, v134
	v_cndmask_b32_e32 v134, 0, v208, vcc
	v_add_u32_e32 v170, s14, v132
	s_addc_u32 s23, s41, 0
	s_lshl_b32 s14, s14, 1
	v_ldexp_f32 v133, v133, v134
	s_add_u32 s22, s22, s14
	v_mul_f32_e32 v169, 0.15915494, v133
	s_addc_u32 s23, s23, 0
	v_ashrrev_i32_e32 v133, 31, v132
	v_lshl_add_u64 v[154:155], v[132:133], 1, s[22:23]
	s_or_b32 s22, s42, s75
	s_ashr_i32 s23, s22, 31
	s_lshl_b64 s[22:23], s[22:23], 1
	s_add_u32 s42, s83, s22
	v_mov_b32_e32 v131, 0x3db504f3
	s_addc_u32 s43, s84, s23
	s_nor_b64 s[22:23], s[36:37], s[2:3]
	v_cndmask_b32_e64 v156, 1.0, v131, s[38:39]
	v_add_u32_e32 v168, s90, v130
	v_and_b32_e32 v173, 0x1fff, v160
	s_mov_b64 s[2:3], -1
	s_and_b64 vcc, exec, s[22:23]
	s_cbranch_vccz .LBB0_506
	v_ashrrev_i32_e32 v174, 13, v160
	s_and_b64 vcc, exec, s[12:13]
	s_cbranch_vccz .LBB0_503
	s_and_b64 vcc, exec, s[56:57]
	s_cbranch_vccz .LBB0_496
	s_andn2_b64 vcc, exec, s[54:55]
	s_cbranch_vccnz .LBB0_493
	v_mul_f32_e32 v132, 0xbfb8aa3b, v126
	v_mul_f32_e32 v133, 0xbfb8aa3b, v127
	v_mul_f32_e32 v134, 0xbfb8aa3b, v128
	v_mul_f32_e32 v135, 0xbfb8aa3b, v129
	v_exp_f32_e32 v132, v132
	v_exp_f32_e32 v133, v133
	v_exp_f32_e32 v134, v134
	v_exp_f32_e32 v135, v135
	v_mul_f32_e32 v136, 0xbfb8aa3b, v120
	v_pk_add_f32 v[132:133], v[132:133], 1.0 op_sel_hi:[1,0]
	v_mul_f32_e32 v137, 0xbfb8aa3b, v121
	v_pk_add_f32 v[134:135], v[134:135], 1.0 op_sel_hi:[1,0]
	v_rcp_f32_e32 v132, v132
	v_rcp_f32_e32 v133, v133
	v_rcp_f32_e32 v134, v134
	v_rcp_f32_e32 v135, v135
	v_exp_f32_e32 v136, v136
	v_pk_mul_f32 v[132:133], v[126:127], v[132:133]
	v_exp_f32_e32 v137, v137
	v_pk_mul_f32 v[134:135], v[128:129], v[134:135]
	v_cvt_pk_bf16_f32 v132, v132, v133
	v_ashrrev_i32_e32 v161, 31, v160
	v_cvt_pk_bf16_f32 v133, v134, v135
	v_mul_f32_e32 v134, 0xbfb8aa3b, v118
	v_mul_f32_e32 v135, 0xbfb8aa3b, v119
	v_exp_f32_e32 v134, v134
	v_exp_f32_e32 v135, v135
	v_pk_add_f32 v[136:137], v[136:137], 1.0 op_sel_hi:[1,0]
	v_lshlrev_b64 v[130:131], 11, v[160:161]
	v_rcp_f32_e32 v136, v136
	v_pk_add_f32 v[134:135], v[134:135], 1.0 op_sel_hi:[1,0]
	v_rcp_f32_e32 v137, v137
	v_rcp_f32_e32 v134, v134
	v_rcp_f32_e32 v135, v135
	v_lshl_add_u64 v[130:131], v[158:159], 0, v[130:131]
	v_pk_mul_f32 v[136:137], v[120:121], v[136:137]
	s_mov_b64 s[2:3], 0
	v_pk_mul_f32 v[134:135], v[118:119], v[134:135]
	s_nop 0
	v_cvt_pk_bf16_f32 v134, v134, v135
	v_cvt_pk_bf16_f32 v135, v136, v137
	global_store_dwordx4 v[130:131], v[132:135], off
	v_mul_f32_e32 v136, 0xbfb8aa3b, v116
	v_mul_f32_e32 v137, 0xbfb8aa3b, v117
	v_mul_f32_e32 v132, 0xbfb8aa3b, v122
	v_mul_f32_e32 v133, 0xbfb8aa3b, v123
	v_mul_f32_e32 v134, 0xbfb8aa3b, v124
	v_mul_f32_e32 v135, 0xbfb8aa3b, v125
	v_exp_f32_e32 v132, v132
	v_exp_f32_e32 v133, v133
	v_exp_f32_e32 v134, v134
	v_exp_f32_e32 v135, v135
	v_exp_f32_e32 v136, v136
	v_pk_add_f32 v[132:133], v[132:133], 1.0 op_sel_hi:[1,0]
	v_exp_f32_e32 v137, v137
	v_pk_add_f32 v[134:135], v[134:135], 1.0 op_sel_hi:[1,0]
	v_rcp_f32_e32 v132, v132
	v_rcp_f32_e32 v133, v133
	v_rcp_f32_e32 v134, v134
	v_rcp_f32_e32 v135, v135
	v_pk_add_f32 v[136:137], v[136:137], 1.0 op_sel_hi:[1,0]
	v_pk_mul_f32 v[132:133], v[122:123], v[132:133]
	v_rcp_f32_e32 v136, v136
	v_pk_mul_f32 v[134:135], v[124:125], v[134:135]
	v_cvt_pk_bf16_f32 v132, v132, v133
	v_rcp_f32_e32 v137, v137
	v_cvt_pk_bf16_f32 v133, v134, v135
	v_mul_f32_e32 v134, 0xbfb8aa3b, v114
	v_mul_f32_e32 v135, 0xbfb8aa3b, v115
	v_exp_f32_e32 v134, v134
	v_exp_f32_e32 v135, v135
	v_pk_mul_f32 v[136:137], v[116:117], v[136:137]
	v_pk_add_f32 v[134:135], v[134:135], 1.0 op_sel_hi:[1,0]
	s_nop 0
	v_rcp_f32_e32 v134, v134
	v_rcp_f32_e32 v135, v135
	s_nop 0
	v_pk_mul_f32 v[134:135], v[114:115], v[134:135]
	s_nop 0
	v_cvt_pk_bf16_f32 v134, v134, v135
	v_cvt_pk_bf16_f32 v135, v136, v137
	global_store_dwordx4 v[130:131], v[132:135], off offset:256
